# v33 + P10 also reuses the MoE tile table that the dispatch phase (P9) left in LDS (first table rebuild skipped)
# speedup vs baseline: 1.0187x; 1.0041x over previous
.LBB0_1592:
	v_readlane_b32 s2, v254, 9
	v_readlane_b32 s3, v254, 10
	s_cmp_lt_i32 s2, 11
	s_cselect_b64 s[2:3], -1, 0
	s_and_b64 s[10:11], s[2:3], s[0:1]
	s_andn2_b64 vcc, exec, s[10:11]
	s_cbranch_vccnz .LBB0_1858
	s_mov_b64 s[0:1], exec
	v_readlane_b32 s2, v254, 4
	v_readlane_b32 s3, v254, 5
	s_and_b64 s[2:3], s[0:1], s[2:3]
	s_mov_b64 exec, s[2:3]
	s_branch .LBB0_1609
	v_mov_b32_e32 v195, 0
	s_waitcnt vmcnt(0)
	v_lshl_add_u64 v[2:3], s[50:51], 0, v[194:195]
	v_add_co_u32_e32 v2, vcc, 0x8000, v2
	v_readlane_b32 s2, v254, 2
	s_nop 0
	v_addc_co_u32_e32 v3, vcc, 0, v3, vcc
	global_load_dword v1, v[2:3], off sc1
	v_mbcnt_lo_u32_b32 v2, -1, 0
	v_mbcnt_hi_u32_b32 v2, -1, v2
	v_and_b32_e32 v3, 64, v2
	v_add_u32_e32 v4, -1, v2
	v_cmp_lt_i32_e32 vcc, v4, v3
	v_add_u32_e32 v5, -2, v2
	v_readlane_b32 s3, v254, 3
	v_cndmask_b32_e32 v4, v4, v2, vcc
	v_lshlrev_b32_e32 v6, 2, v4
	v_cmp_lt_i32_e32 vcc, v5, v3
	v_add_u32_e32 v7, -4, v2
	v_add_u32_e32 v8, -8, v2
	v_cndmask_b32_e32 v5, v5, v2, vcc
	v_lshlrev_b32_e32 v5, 2, v5
	v_cmp_lt_i32_e32 vcc, v7, v3
	v_add_u32_e32 v9, -16, v2
	v_subrev_u32_e32 v10, 32, v2
	v_cndmask_b32_e32 v7, v7, v2, vcc
	v_cmp_lt_u32_e32 vcc, 1, v0
	v_lshlrev_b32_e32 v12, 2, v7
	s_waitcnt vmcnt(0)
	v_add_u32_e32 v4, 0xff, v1
	v_ashrrev_i32_e32 v4, 8, v4
	ds_bpermute_b32 v6, v6, v4
	s_waitcnt lgkmcnt(0)
	v_cndmask_b32_e64 v6, v6, 0, s[2:3]
	v_add_u32_e32 v11, v6, v4
	ds_bpermute_b32 v5, v5, v11
	s_waitcnt lgkmcnt(0)
	v_cndmask_b32_e32 v7, 0, v5, vcc
	v_add_u32_e32 v5, v7, v11
	ds_bpermute_b32 v11, v12, v5
	v_cmp_lt_i32_e32 vcc, v8, v3
	s_nop 1
	v_cndmask_b32_e32 v8, v8, v2, vcc
	v_cmp_lt_u32_e32 vcc, 3, v0
	v_lshlrev_b32_e32 v12, 2, v8
	s_waitcnt lgkmcnt(0)
	v_cndmask_b32_e32 v8, 0, v11, vcc
	v_add_u32_e32 v5, v8, v5
	ds_bpermute_b32 v11, v12, v5
	v_cmp_lt_i32_e32 vcc, v9, v3
	s_nop 1
	v_cndmask_b32_e32 v9, v9, v2, vcc
	v_cmp_lt_u32_e32 vcc, 7, v0
	v_lshlrev_b32_e32 v12, 2, v9
	s_waitcnt lgkmcnt(0)
	v_cndmask_b32_e32 v9, 0, v11, vcc
	v_add_u32_e32 v5, v9, v5
	ds_bpermute_b32 v11, v12, v5
	v_cmp_lt_i32_e32 vcc, v10, v3
	s_nop 1
	v_cndmask_b32_e32 v2, v10, v2, vcc
	v_cmp_lt_u32_e32 vcc, 15, v0
	v_lshlrev_b32_e32 v2, 2, v2
	s_waitcnt lgkmcnt(0)
	v_cndmask_b32_e32 v10, 0, v11, vcc
	v_add_u32_e32 v3, v10, v5
	ds_bpermute_b32 v2, v2, v3
	v_cmp_lt_u32_e32 vcc, 31, v0
	v_add_u32_e32 v5, 0, v194
	v_add_u32_e32 v12, 0x20b20, v5
	s_waitcnt lgkmcnt(0)
	v_cndmask_b32_e32 v11, 0, v2, vcc
	v_add_u32_e32 v5, v11, v3
	v_sub_u32_e32 v2, v5, v4
	v_lshlrev_b32_e32 v2, 8, v2
	v_cmp_lt_i32_e32 vcc, 0, v4
	ds_write_b32 v12, v2
	s_and_saveexec_b64 s[2:3], vcc
	s_cbranch_execz .LBB0_1607
	v_cmp_ne_u32_e32 vcc, 1, v4
	s_mov_b64 s[6:7], -1
	s_and_saveexec_b64 s[4:5], vcc
	s_cbranch_execz .LBB0_1604
	v_add_u32_e32 v2, -2, v4
	v_lshrrev_b32_e32 v3, 1, v2
	v_cmp_lt_u32_e32 vcc, 13, v2
	v_mov_b32_e32 v2, 0
	s_mov_b32 s7, 1
	v_add_u32_e32 v12, 1, v3
	s_mov_b32 s14, 0
	v_mov_b32_e32 v3, 1
	v_mov_b32_e32 v15, v2
	s_and_saveexec_b64 s[8:9], vcc
	s_cbranch_execz .LBB0_1600
	v_add_u32_e32 v2, v6, v7
	v_add3_u32 v2, v2, v8, v9
	v_add3_u32 v2, v2, v10, v11
	v_lshl_add_u32 v2, v2, 2, 0
	v_and_b32_e32 v13, -8, v12
	v_add_u32_e32 v14, 0x20000, v2
	s_mov_b64 s[12:13], 0
	s_mov_b32 s6, 0
